# drop the epilogue-alignment rendezvous of the two wave halves in the expert GEMMs (leading half starts its epilogue while the lagging half finishes its last MMA segment)
# baseline (speedup 1.0000x reference)
; #define PG8_STAGEB(bufoff, gbase) glds2(voffB, (gbase), voffB, (gbase) + qstep, ldsb + (bufoff))
; #define PG8_STAGEA(bufoff, rowb, v, h, kb) do { if constexpr (GATHER) glds2((v)[h][0], Ab + (kb), (v)[h][1], Ab + (kb), ldsb + (bufoff)); \
;         else glds2(voffA, Ab + (rowb) + (h) * hstep + (kb), voffA, Ab + (rowb) + (h) * hstep + qstep + (kb), ldsb + (bufoff)); } while (0)
; #define PG8_LDA(dst, b, h) do { _Pragma("unroll") for (int m = 0; m < 4; ++m) _Pragma("unroll") for (int k = 0; k < 2; ++k) dst[m][k] = *(const PG8_LAS bf16x8*)(lds + PG8_SA(b, h) + aoff + m * 2048 + k * 1024); } while (0)
; #define PG8_LDB(dst, b, h) do { _Pragma("unroll") for (int n = 0; n < 2; ++n) _Pragma("unroll") for (int k = 0; k < 2; ++k) dst[n][k] = *(const PG8_LAS bf16x8*)(lds + PG8_SB(b, h) + boff + n * 2048 + k * 1024); } while (0)
; #define PG8_WAIT_V(n) asm volatile("s_waitcnt vmcnt(" #n ")" ::: "memory")
; #define PG8_WAIT_L(n) asm volatile("s_waitcnt lgkmcnt(" #n ")" ::: "memory")
; #define PG8_BAR __builtin_amdgcn_s_barrier()
; #define PG8_SCHED __builtin_amdgcn_sched_barrier(0)
; template <class Epi, bool GATHER, int MODE, bool SPLIT = false>
; __device__ __forceinline__ void gemm_phase(PG8_LAS unsigned char* lds, const Gemm g, const Order& S, const Epi& E) {
;     ...
;         const bool has_next = S.next(ui + 1, nxt);
;         const char* nB = has_next ? (const char*)g.Bt + (size_t)nxt.e * g.bstride + (size_t)nxt.pn * tstep : cB;
;         const size_t nAr = has_next ? (size_t)nxt.pm * tstep : cAr;
;     ...
;             const size_t k1 = (size_t)(nt - 1) * kstep;
;             PG8_LDB(B0, 0, 0); PG8_LDB(B1, 0, 1); PG8_SCHED; PG8_LDA(At, 0, 0); PG8_STAGEA(PG8_SA(1, 1), cAr, cv, 1, k1);
;             PG8_WAIT_V(8); PG8_WAIT_L(0); PG8_BAR; PG8_MMA(0, 0, At, B0); PG8_MMA(0, 1, At, B1); PG8_BAR; PG8_SCHED;
;             PG8_LDA(At, 0, 1); PG8_STAGEB(PG8_SB(0, 0), nB); PG8_STAGEB(PG8_SB(0, 1), nB + hstep); PG8_STAGEA(PG8_SA(0, 0), nAr, nv, 0, 0);
;             PG8_WAIT_V(8); PG8_WAIT_L(0); PG8_BAR; PG8_MMA(1, 0, At, B0); PG8_MMA(1, 1, At, B1); PG8_BAR; PG8_SCHED;
.Lp8_nonext:
	ds_read_b128 v[140:143], v179
	ds_read_b128 v[144:147], v179 offset:1024
	ds_read_b128 v[148:151], v179 offset:2048
	ds_read_b128 v[152:155], v179 offset:3072
	ds_read_b128 v[156:159], v180
	ds_read_b128 v[130:133], v180 offset:1024
	ds_read_b128 v[192:195], v180 offset:2048
	ds_read_b128 v[134:137], v180 offset:3072
	s_ashr_i32 s29, s28, 31
	s_lshl_b64 s[30:31], s[28:29], 23
	s_add_u32 s11, s41, s30
	s_addc_u32 s29, s42, s31
	s_ashr_i32 s27, s26, 31
	s_lshl_b64 s[30:31], s[26:27], 19
	s_add_u32 s30, s11, s30
	s_addc_u32 s31, s29, s31
	s_and_b64 s[4:5], s[4:5], exec
	s_cselect_b32 s5, s31, s35
	s_cselect_b32 s4, s30, s34
	ds_read_b128 v[196:199], v181
	ds_read_b128 v[200:203], v181 offset:1024
	ds_read_b128 v[204:207], v181 offset:2048
	ds_read_b128 v[208:211], v181 offset:3072
	ds_read_b128 v[212:215], v181 offset:4096
	ds_read_b128 v[216:219], v181 offset:5120
	ds_read_b128 v[220:223], v181 offset:6144
	ds_read_b128 v[224:227], v181 offset:7168
	s_mov_b32 s11, m0
	s_mov_b32 m0, s62
	s_nop 0
	global_load_lds_dwordx4 v189, s[20:21]
	s_mov_b32 m0, s63
	s_nop 0
	global_load_lds_dwordx4 v190, s[20:21]
	s_mov_b32 m0, s11
	s_waitcnt vmcnt(8)
	s_waitcnt lgkmcnt(0)
	s_barrier
	s_setprio 1
	s_waitcnt lgkmcnt(7)
	v_mfma_i32_16x16x64_i8 v[126:129], v[140:143], v[196:199], v[126:129]
	v_mfma_i32_16x16x64_i8 v[122:125], v[148:151], v[196:199], v[122:125]
	s_waitcnt lgkmcnt(5)
	v_mfma_i32_16x16x64_i8 v[118:121], v[140:143], v[204:207], v[118:121]
	v_mfma_i32_16x16x64_i8 v[106:109], v[148:151], v[204:207], v[106:109]
	s_waitcnt lgkmcnt(3)
	v_mfma_i32_16x16x64_i8 v[102:105], v[140:143], v[212:215], v[102:105]
	v_mfma_i32_16x16x64_i8 v[90:93], v[148:151], v[212:215], v[90:93]
	s_waitcnt lgkmcnt(1)
	v_mfma_i32_16x16x64_i8 v[86:89], v[140:143], v[220:223], v[86:89]
	v_mfma_i32_16x16x64_i8 v[74:77], v[148:151], v[220:223], v[74:77]
	v_mfma_i32_16x16x64_i8 v[126:129], v[144:147], v[200:203], v[126:129]
	v_mfma_i32_16x16x64_i8 v[122:125], v[152:155], v[200:203], v[122:125]
	v_mfma_i32_16x16x64_i8 v[118:121], v[144:147], v[208:211], v[118:121]
	v_mfma_i32_16x16x64_i8 v[106:109], v[152:155], v[208:211], v[106:109]
	v_mfma_i32_16x16x64_i8 v[102:105], v[144:147], v[216:219], v[102:105]
	v_mfma_i32_16x16x64_i8 v[90:93], v[152:155], v[216:219], v[90:93]
	s_waitcnt lgkmcnt(0)
	v_mfma_i32_16x16x64_i8 v[86:89], v[144:147], v[224:227], v[86:89]
	v_mfma_i32_16x16x64_i8 v[74:77], v[152:155], v[224:227], v[74:77]
	s_setprio 0
	s_setprio 1
	v_mfma_i32_16x16x64_i8 v[114:117], v[156:159], v[196:199], v[114:117]
	v_mfma_i32_16x16x64_i8 v[110:113], v[192:195], v[196:199], v[110:113]
	v_mfma_i32_16x16x64_i8 v[98:101], v[156:159], v[204:207], v[98:101]
	v_mfma_i32_16x16x64_i8 v[94:97], v[192:195], v[204:207], v[94:97]
	v_mfma_i32_16x16x64_i8 v[82:85], v[156:159], v[212:215], v[82:85]
	v_mfma_i32_16x16x64_i8 v[78:81], v[192:195], v[212:215], v[78:81]
	v_mfma_i32_16x16x64_i8 v[70:73], v[156:159], v[220:223], v[70:73]
	v_mfma_i32_16x16x64_i8 v[66:69], v[192:195], v[220:223], v[66:69]
	s_nop 0
	v_mfma_i32_16x16x64_i8 v[114:117], v[130:133], v[200:203], v[114:117]
	v_mfma_i32_16x16x64_i8 v[110:113], v[134:137], v[200:203], v[110:113]
	v_mfma_i32_16x16x64_i8 v[98:101], v[130:133], v[208:211], v[98:101]
	v_mfma_i32_16x16x64_i8 v[94:97], v[134:137], v[208:211], v[94:97]
	v_mfma_i32_16x16x64_i8 v[82:85], v[130:133], v[216:219], v[82:85]
	v_mfma_i32_16x16x64_i8 v[78:81], v[134:137], v[216:219], v[78:81]
	v_mfma_i32_16x16x64_i8 v[70:73], v[130:133], v[224:227], v[70:73]
	v_mfma_i32_16x16x64_i8 v[66:69], v[134:137], v[224:227], v[66:69]
	s_setprio 0
	s_barrier
	s_add_u32 s34, s4, 0x20000
	ds_read_b128 v[196:199], v181 offset:16384
	ds_read_b128 v[200:203], v181 offset:17408
	ds_read_b128 v[204:207], v181 offset:18432
	ds_read_b128 v[208:211], v181 offset:19456
	ds_read_b128 v[212:215], v181 offset:20480
	ds_read_b128 v[216:219], v181 offset:21504
	ds_read_b128 v[220:223], v181 offset:22528
	ds_read_b128 v[224:227], v181 offset:23552
	s_addc_u32 s35, s5, 0
	s_mov_b32 s11, m0
	s_mov_b32 m0, s49
	s_nop 0
	global_load_lds_dwordx4 v168, s[4:5]
	s_mov_b32 m0, s50
	s_nop 0
	global_load_lds_dwordx4 v168, s[34:35]
	s_mov_b32 m0, s11
	s_add_u32 s34, s4, 0x40000
	s_addc_u32 s35, s5, 0
	s_add_u32 s36, s4, 0x60000
	s_addc_u32 s37, s5, 0
	s_mov_b32 s11, m0
	s_mov_b32 m0, s51
	s_nop 0
	global_load_lds_dwordx4 v168, s[34:35]
	s_mov_b32 m0, s52
	s_nop 0
	global_load_lds_dwordx4 v168, s[36:37]
	s_mov_b32 m0, s11
	s_nop 0
	s_mov_b32 s11, m0
	s_mov_b32 m0, s43
	s_nop 0
	global_load_lds_dwordx4 v184, s[6:7]
	s_mov_b32 m0, s53
	s_nop 0
	global_load_lds_dwordx4 v185, s[6:7]
	s_mov_b32 m0, s11
	s_waitcnt vmcnt(8)
	s_waitcnt lgkmcnt(0)
	s_barrier
; #define PG8_STAGEB(bufoff, gbase) glds2(voffB, (gbase), voffB, (gbase) + qstep, ldsb + (bufoff))
; #define PG8_STAGEA(bufoff, rowb, v, h, kb) do { if constexpr (GATHER) glds2((v)[h][0], Ab + (kb), (v)[h][1], Ab + (kb), ldsb + (bufoff)); \
;         else glds2(voffA, Ab + (rowb) + (h) * hstep + (kb), voffA, Ab + (rowb) + (h) * hstep + qstep + (kb), ldsb + (bufoff)); } while (0)
; #define PG8_LDA(dst, b, h) do { _Pragma("unroll") for (int m = 0; m < 4; ++m) _Pragma("unroll") for (int k = 0; k < 2; ++k) dst[m][k] = *(const PG8_LAS bf16x8*)(lds + PG8_SA(b, h) + aoff + m * 2048 + k * 1024); } while (0)
; #define PG8_LDB(dst, b, h) do { _Pragma("unroll") for (int n = 0; n < 2; ++n) _Pragma("unroll") for (int k = 0; k < 2; ++k) dst[n][k] = *(const PG8_LAS bf16x8*)(lds + PG8_SB(b, h) + boff + n * 2048 + k * 1024); } while (0)
; #define PG8_WAIT_V(n) asm volatile("s_waitcnt vmcnt(" #n ")" ::: "memory")
; #define PG8_WAIT_L(n) asm volatile("s_waitcnt lgkmcnt(" #n ")" ::: "memory")
; #define PG8_BAR __builtin_amdgcn_s_barrier()
; #define PG8_SCHED __builtin_amdgcn_sched_barrier(0)
; template <class Epi, bool GATHER, int MODE, bool SPLIT = false>
; __device__ __forceinline__ void gemm_phase(PG8_LAS unsigned char* lds, const Gemm g, const Order& S, const Epi& E) {
;     ...
;             PG8_WAIT_V(8); PG8_WAIT_L(0); PG8_BAR; PG8_MMA(1, 0, At, B0); PG8_MMA(1, 1, At, B1); PG8_BAR; PG8_SCHED;
;             PG8_LDB(B0, 1, 0); PG8_LDB(B1, 1, 1); PG8_SCHED; PG8_LDA(At, 1, 0); PG8_STAGEA(PG8_SA(0, 1), nAr, nv, 1, 0);
;             PG8_WAIT_V(8); PG8_WAIT_L(0); PG8_BAR; PG8_MMA(0, 0, At, B0); PG8_MMA(0, 1, At, B1); PG8_BAR; PG8_SCHED;
;             PG8_LDA(At, 1, 1); PG8_STAGEB(PG8_SB(1, 0), nB + kstep); PG8_STAGEB(PG8_SB(1, 1), nB + hstep + kstep); PG8_STAGEA(PG8_SA(1, 0), nAr, nv, 0, kstep);
	s_setprio 1
	s_waitcnt lgkmcnt(7)
	v_mfma_i32_16x16x64_i8 v[62:65], v[140:143], v[196:199], v[62:65]
	v_mfma_i32_16x16x64_i8 v[58:61], v[148:151], v[196:199], v[58:61]
	s_waitcnt lgkmcnt(5)
	v_mfma_i32_16x16x64_i8 v[46:49], v[140:143], v[204:207], v[46:49]
	v_mfma_i32_16x16x64_i8 v[42:45], v[148:151], v[204:207], v[42:45]
	s_waitcnt lgkmcnt(3)
	v_mfma_i32_16x16x64_i8 v[38:41], v[140:143], v[212:215], v[38:41]
	v_mfma_i32_16x16x64_i8 v[34:37], v[148:151], v[212:215], v[34:37]
	s_waitcnt lgkmcnt(1)
	v_mfma_i32_16x16x64_i8 v[22:25], v[140:143], v[220:223], v[22:25]
	v_mfma_i32_16x16x64_i8 v[18:21], v[148:151], v[220:223], v[18:21]
	v_mfma_i32_16x16x64_i8 v[62:65], v[144:147], v[200:203], v[62:65]
	v_mfma_i32_16x16x64_i8 v[58:61], v[152:155], v[200:203], v[58:61]
	v_mfma_i32_16x16x64_i8 v[46:49], v[144:147], v[208:211], v[46:49]
	v_mfma_i32_16x16x64_i8 v[42:45], v[152:155], v[208:211], v[42:45]
	v_mfma_i32_16x16x64_i8 v[38:41], v[144:147], v[216:219], v[38:41]
	v_mfma_i32_16x16x64_i8 v[34:37], v[152:155], v[216:219], v[34:37]
	s_waitcnt lgkmcnt(0)
	v_mfma_i32_16x16x64_i8 v[22:25], v[144:147], v[224:227], v[22:25]
	v_mfma_i32_16x16x64_i8 v[18:21], v[152:155], v[224:227], v[18:21]
	s_setprio 0
	s_setprio 1
	v_mfma_i32_16x16x64_i8 v[54:57], v[156:159], v[196:199], v[54:57]
	v_mfma_i32_16x16x64_i8 v[50:53], v[192:195], v[196:199], v[50:53]
	v_mfma_i32_16x16x64_i8 v[30:33], v[156:159], v[204:207], v[30:33]
	v_mfma_i32_16x16x64_i8 v[26:29], v[192:195], v[204:207], v[26:29]
	v_mfma_i32_16x16x64_i8 v[14:17], v[156:159], v[212:215], v[14:17]
	v_mfma_i32_16x16x64_i8 v[10:13], v[192:195], v[212:215], v[10:13]
	v_mfma_i32_16x16x64_i8 v[6:9], v[156:159], v[220:223], v[6:9]
	v_mfma_i32_16x16x64_i8 v[2:5], v[192:195], v[220:223], v[2:5]
	s_nop 0
	v_mfma_i32_16x16x64_i8 v[54:57], v[130:133], v[200:203], v[54:57]
	v_mfma_i32_16x16x64_i8 v[50:53], v[134:137], v[200:203], v[50:53]
	v_mfma_i32_16x16x64_i8 v[30:33], v[130:133], v[208:211], v[30:33]
	v_mfma_i32_16x16x64_i8 v[26:29], v[134:137], v[208:211], v[26:29]
	v_mfma_i32_16x16x64_i8 v[14:17], v[130:133], v[216:219], v[14:17]
	v_mfma_i32_16x16x64_i8 v[10:13], v[134:137], v[216:219], v[10:13]
	v_mfma_i32_16x16x64_i8 v[6:9], v[130:133], v[224:227], v[6:9]
	v_mfma_i32_16x16x64_i8 v[2:5], v[134:137], v[224:227], v[2:5]
	s_setprio 0
	s_barrier
	ds_read_b128 v[130:133], v182
	ds_read_b128 v[134:137], v182 offset:1024
	ds_read_b128 v[140:143], v182 offset:2048
	ds_read_b128 v[144:147], v182 offset:3072
	ds_read_b128 v[148:151], v138
	ds_read_b128 v[152:155], v138 offset:1024
	ds_read_b128 v[156:159], v138 offset:2048
	ds_read_b128 v[190:193], v138 offset:3072
	ds_read_b128 v[194:197], v181 offset:32768
	ds_read_b128 v[198:201], v181 offset:33792
	ds_read_b128 v[202:205], v181 offset:34816
	ds_read_b128 v[206:209], v181 offset:35840
	ds_read_b128 v[210:213], v181 offset:36864
	ds_read_b128 v[214:217], v181 offset:37888
	ds_read_b128 v[218:221], v181 offset:38912
	ds_read_b128 v[222:225], v181 offset:39936
	s_mov_b32 s11, m0
	s_mov_b32 m0, s54
	s_nop 0
	global_load_lds_dwordx4 v186, s[6:7]
	s_mov_b32 m0, s55
	s_nop 0
	global_load_lds_dwordx4 v187, s[6:7]
	s_mov_b32 m0, s11
	s_waitcnt vmcnt(8)
	s_waitcnt lgkmcnt(0)
	s_barrier
	s_setprio 1
	s_waitcnt lgkmcnt(7)
	v_mfma_i32_16x16x64_i8 v[126:129], v[130:133], v[194:197], v[126:129]
	v_mfma_i32_16x16x64_i8 v[122:125], v[140:143], v[194:197], v[122:125]
	s_waitcnt lgkmcnt(5)
	v_mfma_i32_16x16x64_i8 v[118:121], v[130:133], v[202:205], v[118:121]
	v_mfma_i32_16x16x64_i8 v[106:109], v[140:143], v[202:205], v[106:109]
	s_waitcnt lgkmcnt(3)
	v_mfma_i32_16x16x64_i8 v[102:105], v[130:133], v[210:213], v[102:105]
	v_mfma_i32_16x16x64_i8 v[90:93], v[140:143], v[210:213], v[90:93]
	s_waitcnt lgkmcnt(1)
	v_mfma_i32_16x16x64_i8 v[86:89], v[130:133], v[218:221], v[86:89]
	v_mfma_i32_16x16x64_i8 v[74:77], v[140:143], v[218:221], v[74:77]
	v_mfma_i32_16x16x64_i8 v[126:129], v[134:137], v[198:201], v[126:129]
	v_mfma_i32_16x16x64_i8 v[122:125], v[144:147], v[198:201], v[122:125]
	v_mfma_i32_16x16x64_i8 v[118:121], v[134:137], v[206:209], v[118:121]
	v_mfma_i32_16x16x64_i8 v[106:109], v[144:147], v[206:209], v[106:109]
	v_mfma_i32_16x16x64_i8 v[102:105], v[134:137], v[214:217], v[102:105]
	v_mfma_i32_16x16x64_i8 v[90:93], v[144:147], v[214:217], v[90:93]
	s_waitcnt lgkmcnt(0)
	v_mfma_i32_16x16x64_i8 v[86:89], v[134:137], v[222:225], v[86:89]
	v_mfma_i32_16x16x64_i8 v[74:77], v[144:147], v[222:225], v[74:77]
	s_setprio 0
	s_setprio 1
	v_mfma_i32_16x16x64_i8 v[114:117], v[148:151], v[194:197], v[114:117]
	v_mfma_i32_16x16x64_i8 v[110:113], v[156:159], v[194:197], v[110:113]
	v_mfma_i32_16x16x64_i8 v[98:101], v[148:151], v[202:205], v[98:101]
	v_mfma_i32_16x16x64_i8 v[94:97], v[156:159], v[202:205], v[94:97]
	v_mfma_i32_16x16x64_i8 v[82:85], v[148:151], v[210:213], v[82:85]
	v_mfma_i32_16x16x64_i8 v[78:81], v[156:159], v[210:213], v[78:81]
	v_mfma_i32_16x16x64_i8 v[70:73], v[148:151], v[218:221], v[70:73]
	v_mfma_i32_16x16x64_i8 v[66:69], v[156:159], v[218:221], v[66:69]
	s_nop 0
	v_mfma_i32_16x16x64_i8 v[114:117], v[152:155], v[198:201], v[114:117]
	v_mfma_i32_16x16x64_i8 v[110:113], v[190:193], v[198:201], v[110:113]
	v_mfma_i32_16x16x64_i8 v[98:101], v[152:155], v[206:209], v[98:101]
	v_mfma_i32_16x16x64_i8 v[94:97], v[190:193], v[206:209], v[94:97]
	v_mfma_i32_16x16x64_i8 v[82:85], v[152:155], v[214:217], v[82:85]
	v_mfma_i32_16x16x64_i8 v[78:81], v[190:193], v[214:217], v[78:81]
	v_mfma_i32_16x16x64_i8 v[70:73], v[152:155], v[222:225], v[70:73]
	v_mfma_i32_16x16x64_i8 v[66:69], v[190:193], v[222:225], v[66:69]
	s_setprio 0
	s_barrier
; #define PG8_STAGEB(bufoff, gbase) glds2(voffB, (gbase), voffB, (gbase) + qstep, ldsb + (bufoff))
; #define PG8_STAGEA(bufoff, rowb, v, h, kb) do { if constexpr (GATHER) glds2((v)[h][0], Ab + (kb), (v)[h][1], Ab + (kb), ldsb + (bufoff)); \
;         else glds2(voffA, Ab + (rowb) + (h) * hstep + (kb), voffA, Ab + (rowb) + (h) * hstep + qstep + (kb), ldsb + (bufoff)); } while (0)
; #define PG8_LDA(dst, b, h) do { _Pragma("unroll") for (int m = 0; m < 4; ++m) _Pragma("unroll") for (int k = 0; k < 2; ++k) dst[m][k] = *(const PG8_LAS bf16x8*)(lds + PG8_SA(b, h) + aoff + m * 2048 + k * 1024); } while (0)
; #define PG8_WAIT_V(n) asm volatile("s_waitcnt vmcnt(" #n ")" ::: "memory")
; #define PG8_WAIT_L(n) asm volatile("s_waitcnt lgkmcnt(" #n ")" ::: "memory")
; #define PG8_BAR __builtin_amdgcn_s_barrier()
; #define PG8_SCHED __builtin_amdgcn_sched_barrier(0)
; template <class Epi, bool GATHER, int MODE, bool SPLIT = false>
; __device__ __forceinline__ void gemm_phase(PG8_LAS unsigned char* lds, const Gemm g, const Order& S, const Epi& E) {
;     ...
;             PG8_LDA(At, 1, 1); PG8_STAGEB(PG8_SB(1, 0), nB + kstep); PG8_STAGEB(PG8_SB(1, 1), nB + hstep + kstep); PG8_STAGEA(PG8_SA(1, 0), nAr, nv, 0, kstep);
;             PG8_WAIT_V(8); PG8_WAIT_L(0); PG8_BAR; PG8_MMA(1, 0, At, B0); PG8_MMA(1, 1, At, B1); PG8_BAR; PG8_SCHED;
;         }
;         if (wr == 0) PG8_BAR;
	s_add_u32 s34, s4, 0x80
	s_addc_u32 s35, s5, 0
	s_add_u32 s36, s4, 0x20080
	ds_read_b128 v[194:197], v181 offset:49152
	ds_read_b128 v[198:201], v181 offset:50176
	ds_read_b128 v[202:205], v181 offset:51200
	ds_read_b128 v[206:209], v181 offset:52224
	ds_read_b128 v[210:213], v181 offset:53248
	ds_read_b128 v[214:217], v181 offset:54272
	ds_read_b128 v[218:221], v181 offset:55296
	ds_read_b128 v[222:225], v181 offset:56320
	s_addc_u32 s37, s5, 0
	s_mov_b32 s11, m0
	s_mov_b32 m0, s56
	s_nop 0
	global_load_lds_dwordx4 v168, s[34:35]
	s_mov_b32 m0, s57
	s_nop 0
	global_load_lds_dwordx4 v168, s[36:37]
	s_mov_b32 m0, s11
	s_add_u32 s34, s4, 0x40080
	s_addc_u32 s35, s5, 0
	s_add_u32 s4, s4, 0x60080
	s_addc_u32 s5, s5, 0
	s_mov_b32 s11, m0
	s_mov_b32 m0, s60
	s_nop 0
	global_load_lds_dwordx4 v168, s[34:35]
	s_mov_b32 m0, s61
	s_nop 0
	global_load_lds_dwordx4 v168, s[4:5]
	s_mov_b32 m0, s11
	s_mov_b32 s4, m0
	s_mov_b32 m0, s58
	s_nop 0
	global_load_lds_dwordx4 v184, s[18:19]
	s_mov_b32 m0, s59
	s_nop 0
	global_load_lds_dwordx4 v185, s[18:19]
	s_mov_b32 m0, s4
	s_waitcnt vmcnt(8)
	s_waitcnt lgkmcnt(0)
	s_barrier
	s_setprio 1
	s_waitcnt lgkmcnt(7)
	v_mfma_i32_16x16x64_i8 v[62:65], v[130:133], v[194:197], v[62:65]
	v_mfma_i32_16x16x64_i8 v[58:61], v[140:143], v[194:197], v[58:61]
	s_waitcnt lgkmcnt(5)
	v_mfma_i32_16x16x64_i8 v[46:49], v[130:133], v[202:205], v[46:49]
	v_mfma_i32_16x16x64_i8 v[42:45], v[140:143], v[202:205], v[42:45]
	s_waitcnt lgkmcnt(3)
	v_mfma_i32_16x16x64_i8 v[38:41], v[130:133], v[210:213], v[38:41]
	v_mfma_i32_16x16x64_i8 v[34:37], v[140:143], v[210:213], v[34:37]
	s_waitcnt lgkmcnt(1)
	v_mfma_i32_16x16x64_i8 v[22:25], v[130:133], v[218:221], v[22:25]
	v_mfma_i32_16x16x64_i8 v[18:21], v[140:143], v[218:221], v[18:21]
	v_mfma_i32_16x16x64_i8 v[62:65], v[134:137], v[198:201], v[62:65]
	v_mfma_i32_16x16x64_i8 v[58:61], v[144:147], v[198:201], v[58:61]
	v_mfma_i32_16x16x64_i8 v[46:49], v[134:137], v[206:209], v[46:49]
	v_mfma_i32_16x16x64_i8 v[42:45], v[144:147], v[206:209], v[42:45]
	v_mfma_i32_16x16x64_i8 v[38:41], v[134:137], v[214:217], v[38:41]
	v_mfma_i32_16x16x64_i8 v[34:37], v[144:147], v[214:217], v[34:37]
	s_waitcnt lgkmcnt(0)
	v_mfma_i32_16x16x64_i8 v[22:25], v[134:137], v[222:225], v[22:25]
	v_mfma_i32_16x16x64_i8 v[18:21], v[144:147], v[222:225], v[18:21]
	s_setprio 0
	s_setprio 1
	v_mfma_i32_16x16x64_i8 v[54:57], v[148:151], v[194:197], v[54:57]
	v_mfma_i32_16x16x64_i8 v[50:53], v[156:159], v[194:197], v[50:53]
	v_mfma_i32_16x16x64_i8 v[30:33], v[148:151], v[202:205], v[30:33]
	v_mfma_i32_16x16x64_i8 v[26:29], v[156:159], v[202:205], v[26:29]
	v_mfma_i32_16x16x64_i8 v[14:17], v[148:151], v[210:213], v[14:17]
	v_mfma_i32_16x16x64_i8 v[10:13], v[156:159], v[210:213], v[10:13]
	v_mfma_i32_16x16x64_i8 v[6:9], v[148:151], v[218:221], v[6:9]
	v_mfma_i32_16x16x64_i8 v[2:5], v[156:159], v[218:221], v[2:5]
	s_nop 0
	v_mfma_i32_16x16x64_i8 v[54:57], v[152:155], v[198:201], v[54:57]
	v_mfma_i32_16x16x64_i8 v[50:53], v[190:193], v[198:201], v[50:53]
	v_mfma_i32_16x16x64_i8 v[30:33], v[152:155], v[206:209], v[30:33]
	v_mfma_i32_16x16x64_i8 v[26:29], v[190:193], v[206:209], v[26:29]
	v_mfma_i32_16x16x64_i8 v[14:17], v[152:155], v[214:217], v[14:17]
	v_mfma_i32_16x16x64_i8 v[10:13], v[190:193], v[214:217], v[10:13]
	v_mfma_i32_16x16x64_i8 v[6:9], v[152:155], v[222:225], v[6:9]
	v_mfma_i32_16x16x64_i8 v[2:5], v[190:193], v[222:225], v[2:5]
	s_setprio 0
	s_nop 0
	s_andn2_b64 vcc, exec, s[22:23]
	s_cbranch_vccnz .LBB0_805
	s_barrier

; #define PG8_STAGEB(bufoff, gbase) glds2(voffB, (gbase), voffB, (gbase) + qstep, ldsb + (bufoff))
; #define PG8_STAGEA(bufoff, rowb, v, h, kb) do { if constexpr (GATHER) glds2((v)[h][0], Ab + (kb), (v)[h][1], Ab + (kb), ldsb + (bufoff)); \
;         else glds2(voffA, Ab + (rowb) + (h) * hstep + (kb), voffA, Ab + (rowb) + (h) * hstep + qstep + (kb), ldsb + (bufoff)); } while (0)
; #define PG8_LDA(dst, b, h) do { _Pragma("unroll") for (int m = 0; m < 4; ++m) _Pragma("unroll") for (int k = 0; k < 2; ++k) dst[m][k] = *(const PG8_LAS bf16x8*)(lds + PG8_SA(b, h) + aoff + m * 2048 + k * 1024); } while (0)
; #define PG8_LDB(dst, b, h) do { _Pragma("unroll") for (int n = 0; n < 2; ++n) _Pragma("unroll") for (int k = 0; k < 2; ++k) dst[n][k] = *(const PG8_LAS bf16x8*)(lds + PG8_SB(b, h) + boff + n * 2048 + k * 1024); } while (0)
; #define PG8_WAIT_V(n) asm volatile("s_waitcnt vmcnt(" #n ")" ::: "memory")
; #define PG8_WAIT_L(n) asm volatile("s_waitcnt lgkmcnt(" #n ")" ::: "memory")
; #define PG8_BAR __builtin_amdgcn_s_barrier()
; #define PG8_SCHED __builtin_amdgcn_sched_barrier(0)
; template <class Epi, bool GATHER, int MODE, bool SPLIT = false>
; __device__ __forceinline__ void gemm_phase(PG8_LAS unsigned char* lds, const Gemm g, const Order& S, const Epi& E) {
;     ...
;             const size_t k1 = (size_t)(t + 1) * kstep, k2 = k1 + kstep, k3 = k2 + kstep;
;             const char* b2 = cB + k2; const char* b3 = cB + k3;
;             PG8_LDB(B0, 0, 0); PG8_LDB(B1, 0, 1); PG8_SCHED; PG8_LDA(At, 0, 0); PG8_STAGEA(PG8_SA(1, 1), cAr, cv, 1, k1);
;             PG8_WAIT_V(8); PG8_WAIT_L(0); PG8_BAR; PG8_MMA(0, 0, At, B0); PG8_MMA(0, 1, At, B1); PG8_BAR; PG8_SCHED;
;             PG8_LDA(At, 0, 1); PG8_STAGEB(PG8_SB(0, 0), b2); PG8_STAGEB(PG8_SB(0, 1), b2 + hstep); PG8_STAGEA(PG8_SA(0, 0), cAr, cv, 0, k2);
;             PG8_WAIT_V(8); PG8_WAIT_L(0); PG8_BAR; PG8_MMA(1, 0, At, B0); PG8_MMA(1, 1, At, B1); PG8_BAR; PG8_SCHED;
;             PG8_LDB(B0, 1, 0); PG8_LDB(B1, 1, 1); PG8_SCHED; PG8_LDA(At, 1, 0); PG8_STAGEA(PG8_SA(0, 1), cAr, cv, 1, k2);
;             PG8_WAIT_V(8); PG8_WAIT_L(0); PG8_BAR; PG8_MMA(0, 0, At, B0); PG8_MMA(0, 1, At, B1); PG8_BAR; PG8_SCHED;
.LBB0_875:
	ds_read_b128 v[26:29], v172
	ds_read_b128 v[30:33], v172 offset:1024
	ds_read_b128 v[18:21], v172 offset:2048
	ds_read_b128 v[22:25], v172 offset:3072
	ds_read_b128 v[10:13], v173
	ds_read_b128 v[14:17], v173 offset:1024
	ds_read_b128 v[2:5], v173 offset:2048
	ds_read_b128 v[6:9], v173 offset:3072
	s_add_u32 s63, s24, s26
	s_addc_u32 s64, s25, s27
	s_add_u32 s28, s63, 0x100
	s_addc_u32 s29, s64, 0
	s_add_u32 s65, s15, s26
	ds_read_b128 v[180:183], v174
	ds_read_b128 v[184:187], v174 offset:1024
	ds_read_b128 v[188:191], v174 offset:2048
	ds_read_b128 v[192:195], v174 offset:3072
	ds_read_b128 v[196:199], v174 offset:4096
	ds_read_b128 v[200:203], v174 offset:5120
	ds_read_b128 v[204:207], v174 offset:6144
	ds_read_b128 v[208:211], v174 offset:7168
	s_addc_u32 s66, s19, s27
	s_add_u32 s70, s65, 0x80
	s_addc_u32 s71, s66, 0
	s_add_u32 s67, s58, s26
	s_addc_u32 s68, s59, s27
	s_add_u32 s80, s67, 0x80
	s_addc_u32 s81, s68, 0
	s_mov_b32 s69, m0
	s_mov_b32 m0, s53
	s_nop 0
	global_load_lds_dwordx4 v167, s[70:71]
	s_mov_b32 m0, s54
	s_nop 0
	global_load_lds_dwordx4 v167, s[80:81]
	s_mov_b32 m0, s69
	s_waitcnt vmcnt(8)
	s_waitcnt lgkmcnt(0)
	s_barrier
	s_setprio 1
	s_waitcnt lgkmcnt(6)
	v_mfma_f32_16x16x128_f8f6f4 v[158:161], v[26:33], v[180:187], v[158:161]
	v_mfma_f32_16x16x128_f8f6f4 v[154:157], v[18:25], v[180:187], v[154:157]
	s_waitcnt lgkmcnt(4)
	v_mfma_f32_16x16x128_f8f6f4 v[150:153], v[26:33], v[188:195], v[150:153]
	v_mfma_f32_16x16x128_f8f6f4 v[146:149], v[18:25], v[188:195], v[146:149]
	s_waitcnt lgkmcnt(2)
	v_mfma_f32_16x16x128_f8f6f4 v[142:145], v[26:33], v[196:203], v[142:145]
	v_mfma_f32_16x16x128_f8f6f4 v[138:141], v[18:25], v[196:203], v[138:141]
	s_waitcnt lgkmcnt(0)
	v_mfma_f32_16x16x128_f8f6f4 v[134:137], v[26:33], v[204:211], v[134:137]
	v_mfma_f32_16x16x128_f8f6f4 v[130:133], v[18:25], v[204:211], v[130:133]
	s_setprio 0
	s_setprio 1
	v_mfma_f32_16x16x128_f8f6f4 v[126:129], v[10:17], v[180:187], v[126:129]
	v_mfma_f32_16x16x128_f8f6f4 v[122:125], v[2:9], v[180:187], v[122:125]
	v_mfma_f32_16x16x128_f8f6f4 v[118:121], v[10:17], v[188:195], v[118:121]
	v_mfma_f32_16x16x128_f8f6f4 v[114:117], v[2:9], v[188:195], v[114:117]
	v_mfma_f32_16x16x128_f8f6f4 v[110:113], v[10:17], v[196:203], v[110:113]
	v_mfma_f32_16x16x128_f8f6f4 v[106:109], v[2:9], v[196:203], v[106:109]
	v_mfma_f32_16x16x128_f8f6f4 v[102:105], v[10:17], v[204:211], v[102:105]
	v_mfma_f32_16x16x128_f8f6f4 v[98:101], v[2:9], v[204:211], v[98:101]
	s_setprio 0
	s_barrier
	s_add_u32 s70, s63, 0x20100
	s_addc_u32 s71, s64, 0
	ds_read_b128 v[180:183], v174 offset:16384
	ds_read_b128 v[184:187], v174 offset:17408
	ds_read_b128 v[188:191], v174 offset:18432
	ds_read_b128 v[192:195], v174 offset:19456
	ds_read_b128 v[196:199], v174 offset:20480
	ds_read_b128 v[200:203], v174 offset:21504
	ds_read_b128 v[204:207], v174 offset:22528
	ds_read_b128 v[208:211], v174 offset:23552
	s_mov_b32 s69, m0
	s_mov_b32 m0, s21
	s_nop 0
	global_load_lds_dwordx4 v166, s[28:29]
	s_mov_b32 m0, s41
	s_nop 0
	global_load_lds_dwordx4 v166, s[70:71]
	s_mov_b32 m0, s69
	s_add_u32 s28, s63, 0x40100
	s_addc_u32 s29, s64, 0
	s_add_u32 s70, s63, 0x60100
	s_addc_u32 s71, s64, 0
	s_mov_b32 s69, m0
	s_mov_b32 m0, s42
	s_nop 0
	global_load_lds_dwordx4 v166, s[28:29]
	s_mov_b32 m0, s43
	s_nop 0
	global_load_lds_dwordx4 v166, s[70:71]
	s_mov_b32 m0, s69
	s_add_u32 s28, s1, s26
	s_addc_u32 s29, s57, s27
	s_add_u32 s80, s28, 0x100
	s_addc_u32 s81, s29, 0
	s_add_u32 s69, s60, s26
	s_addc_u32 s70, s61, s27
	s_add_u32 s82, s69, 0x100
	s_addc_u32 s83, s70, 0
	s_mov_b32 s71, m0
	s_mov_b32 m0, s37
	s_nop 0
	global_load_lds_dwordx4 v167, s[80:81]
	s_mov_b32 m0, s44
	s_nop 0
	global_load_lds_dwordx4 v167, s[82:83]
	s_mov_b32 m0, s71
	s_waitcnt vmcnt(8)
	s_waitcnt lgkmcnt(0)
	s_barrier
	s_setprio 1
	s_waitcnt lgkmcnt(6)
	v_mfma_f32_16x16x128_f8f6f4 v[94:97], v[26:33], v[180:187], v[94:97]
	v_mfma_f32_16x16x128_f8f6f4 v[90:93], v[18:25], v[180:187], v[90:93]
	s_waitcnt lgkmcnt(4)
	v_mfma_f32_16x16x128_f8f6f4 v[86:89], v[26:33], v[188:195], v[86:89]
	v_mfma_f32_16x16x128_f8f6f4 v[82:85], v[18:25], v[188:195], v[82:85]
	s_waitcnt lgkmcnt(2)
	v_mfma_f32_16x16x128_f8f6f4 v[78:81], v[26:33], v[196:203], v[78:81]
	v_mfma_f32_16x16x128_f8f6f4 v[74:77], v[18:25], v[196:203], v[74:77]
	s_waitcnt lgkmcnt(0)
	v_mfma_f32_16x16x128_f8f6f4 v[70:73], v[26:33], v[204:211], v[70:73]
	v_mfma_f32_16x16x128_f8f6f4 v[66:69], v[18:25], v[204:211], v[66:69]
	s_setprio 0
	s_setprio 1
	v_mfma_f32_16x16x128_f8f6f4 v[62:65], v[10:17], v[180:187], v[62:65]
	v_mfma_f32_16x16x128_f8f6f4 v[58:61], v[2:9], v[180:187], v[58:61]
	v_mfma_f32_16x16x128_f8f6f4 v[54:57], v[10:17], v[188:195], v[54:57]
	v_mfma_f32_16x16x128_f8f6f4 v[50:53], v[2:9], v[188:195], v[50:53]
	v_mfma_f32_16x16x128_f8f6f4 v[46:49], v[10:17], v[196:203], v[46:49]
	v_mfma_f32_16x16x128_f8f6f4 v[42:45], v[2:9], v[196:203], v[42:45]
	v_mfma_f32_16x16x128_f8f6f4 v[38:41], v[10:17], v[204:211], v[38:41]
	v_mfma_f32_16x16x128_f8f6f4 v[34:37], v[2:9], v[204:211], v[34:37]
	s_setprio 0
	s_barrier
	ds_read_b128 v[18:21], v175
	ds_read_b128 v[22:25], v175 offset:1024
	ds_read_b128 v[26:29], v175 offset:2048
	ds_read_b128 v[30:33], v175 offset:3072
	ds_read_b128 v[10:13], v176
	ds_read_b128 v[14:17], v176 offset:1024
	ds_read_b128 v[2:5], v176 offset:2048
	ds_read_b128 v[6:9], v176 offset:3072
	ds_read_b128 v[180:183], v174 offset:32768
	ds_read_b128 v[184:187], v174 offset:33792
	ds_read_b128 v[188:191], v174 offset:34816
	ds_read_b128 v[192:195], v174 offset:35840
	ds_read_b128 v[196:199], v174 offset:36864
	ds_read_b128 v[200:203], v174 offset:37888
	ds_read_b128 v[204:207], v174 offset:38912
	ds_read_b128 v[208:211], v174 offset:39936
	s_add_u32 s80, s65, 0x100
	s_addc_u32 s81, s66, 0
	s_add_u32 s66, s67, 0x100
	s_addc_u32 s67, s68, 0
	s_mov_b32 s65, m0
	s_mov_b32 m0, s45
	s_nop 0
	global_load_lds_dwordx4 v167, s[80:81]
	s_mov_b32 m0, s46
	s_nop 0
	global_load_lds_dwordx4 v167, s[66:67]
	s_mov_b32 m0, s65
	s_waitcnt vmcnt(8)
	s_waitcnt lgkmcnt(0)
	s_barrier
; #define PG8_STAGEB(bufoff, gbase) glds2(voffB, (gbase), voffB, (gbase) + qstep, ldsb + (bufoff))
; #define PG8_STAGEA(bufoff, rowb, v, h, kb) do { if constexpr (GATHER) glds2((v)[h][0], Ab + (kb), (v)[h][1], Ab + (kb), ldsb + (bufoff)); \
;         else glds2(voffA, Ab + (rowb) + (h) * hstep + (kb), voffA, Ab + (rowb) + (h) * hstep + qstep + (kb), ldsb + (bufoff)); } while (0)
; #define PG8_LDA(dst, b, h) do { _Pragma("unroll") for (int m = 0; m < 4; ++m) _Pragma("unroll") for (int k = 0; k < 2; ++k) dst[m][k] = *(const PG8_LAS bf16x8*)(lds + PG8_SA(b, h) + aoff + m * 2048 + k * 1024); } while (0)
; #define PG8_LDB(dst, b, h) do { _Pragma("unroll") for (int n = 0; n < 2; ++n) _Pragma("unroll") for (int k = 0; k < 2; ++k) dst[n][k] = *(const PG8_LAS bf16x8*)(lds + PG8_SB(b, h) + boff + n * 2048 + k * 1024); } while (0)
; #define PG8_WAIT_V(n) asm volatile("s_waitcnt vmcnt(" #n ")" ::: "memory")
; #define PG8_WAIT_L(n) asm volatile("s_waitcnt lgkmcnt(" #n ")" ::: "memory")
; #define PG8_BAR __builtin_amdgcn_s_barrier()
; #define PG8_SCHED __builtin_amdgcn_sched_barrier(0)
; template <class Epi, bool GATHER, int MODE, bool SPLIT = false>
; __device__ __forceinline__ void gemm_phase(PG8_LAS unsigned char* lds, const Gemm g, const Order& S, const Epi& E) {
;     ...
;             PG8_LDA(At, 1, 1); PG8_STAGEB(PG8_SB(1, 0), b3); PG8_STAGEB(PG8_SB(1, 1), b3 + hstep); PG8_STAGEA(PG8_SA(1, 0), cAr, cv, 0, k3);
;             PG8_WAIT_V(8); PG8_WAIT_L(0); PG8_BAR; PG8_MMA(1, 0, At, B0); PG8_MMA(1, 1, At, B1); PG8_BAR; PG8_SCHED;
;         }
;         {
;             const size_t k1 = (size_t)(nt - 1) * kstep;
;             PG8_LDB(B0, 0, 0); PG8_LDB(B1, 0, 1); PG8_SCHED; PG8_LDA(At, 0, 0); PG8_STAGEA(PG8_SA(1, 1), cAr, cv, 1, k1);
;             PG8_WAIT_V(8); PG8_WAIT_L(0); PG8_BAR; PG8_MMA(0, 0, At, B0); PG8_MMA(0, 1, At, B1); PG8_BAR; PG8_SCHED;
;             PG8_LDA(At, 0, 1); PG8_STAGEB(PG8_SB(0, 0), nB); PG8_STAGEB(PG8_SB(0, 1), nB + hstep); PG8_STAGEA(PG8_SA(0, 0), nAr, nv, 0, 0);
;             PG8_WAIT_V(8); PG8_WAIT_L(0); PG8_BAR; PG8_MMA(1, 0, At, B0); PG8_MMA(1, 1, At, B1); PG8_BAR; PG8_SCHED;
	s_setprio 1
	s_waitcnt lgkmcnt(6)
	v_mfma_f32_16x16x128_f8f6f4 v[158:161], v[18:25], v[180:187], v[158:161]
	v_mfma_f32_16x16x128_f8f6f4 v[154:157], v[26:33], v[180:187], v[154:157]
	s_waitcnt lgkmcnt(4)
	v_mfma_f32_16x16x128_f8f6f4 v[150:153], v[18:25], v[188:195], v[150:153]
	v_mfma_f32_16x16x128_f8f6f4 v[146:149], v[26:33], v[188:195], v[146:149]
	s_waitcnt lgkmcnt(2)
	v_mfma_f32_16x16x128_f8f6f4 v[142:145], v[18:25], v[196:203], v[142:145]
	v_mfma_f32_16x16x128_f8f6f4 v[138:141], v[26:33], v[196:203], v[138:141]
	s_waitcnt lgkmcnt(0)
	v_mfma_f32_16x16x128_f8f6f4 v[134:137], v[18:25], v[204:211], v[134:137]
	v_mfma_f32_16x16x128_f8f6f4 v[130:133], v[26:33], v[204:211], v[130:133]
	s_setprio 0
	s_setprio 1
	v_mfma_f32_16x16x128_f8f6f4 v[126:129], v[10:17], v[180:187], v[126:129]
	v_mfma_f32_16x16x128_f8f6f4 v[122:125], v[2:9], v[180:187], v[122:125]
	v_mfma_f32_16x16x128_f8f6f4 v[118:121], v[10:17], v[188:195], v[118:121]
	v_mfma_f32_16x16x128_f8f6f4 v[114:117], v[2:9], v[188:195], v[114:117]
	v_mfma_f32_16x16x128_f8f6f4 v[110:113], v[10:17], v[196:203], v[110:113]
	v_mfma_f32_16x16x128_f8f6f4 v[106:109], v[2:9], v[196:203], v[106:109]
	v_mfma_f32_16x16x128_f8f6f4 v[102:105], v[10:17], v[204:211], v[102:105]
	v_mfma_f32_16x16x128_f8f6f4 v[98:101], v[2:9], v[204:211], v[98:101]
	s_setprio 0
	s_barrier
	s_add_u32 s66, s63, 0x180
	s_addc_u32 s67, s64, 0
	s_add_u32 s80, s63, 0x20180
	s_addc_u32 s81, s64, 0
	ds_read_b128 v[180:183], v174 offset:49152
	ds_read_b128 v[184:187], v174 offset:50176
	ds_read_b128 v[188:191], v174 offset:51200
	ds_read_b128 v[192:195], v174 offset:52224
	ds_read_b128 v[196:199], v174 offset:53248
	ds_read_b128 v[200:203], v174 offset:54272
	ds_read_b128 v[204:207], v174 offset:55296
	ds_read_b128 v[208:211], v174 offset:56320
	s_mov_b32 s65, m0
	s_mov_b32 m0, s47
	s_nop 0
	global_load_lds_dwordx4 v166, s[66:67]
	s_mov_b32 m0, s48
	s_nop 0
	global_load_lds_dwordx4 v166, s[80:81]
	s_mov_b32 m0, s65
	s_add_u32 s66, s63, 0x40180
	s_addc_u32 s67, s64, 0
	s_add_u32 s80, s63, 0x60180
	s_addc_u32 s81, s64, 0
	s_add_u32 s28, s28, 0x180
	s_addc_u32 s29, s29, 0
	s_mov_b32 s63, m0
	s_mov_b32 m0, s51
	s_nop 0
	global_load_lds_dwordx4 v166, s[66:67]
	s_mov_b32 m0, s52
	s_nop 0
	global_load_lds_dwordx4 v166, s[80:81]
	s_mov_b32 m0, s63
	s_add_u32 s64, s69, 0x180
	s_addc_u32 s65, s70, 0
	s_mov_b32 s63, m0
	s_mov_b32 m0, s49
	s_nop 0
	global_load_lds_dwordx4 v167, s[28:29]
	s_mov_b32 m0, s50
	s_nop 0
	global_load_lds_dwordx4 v167, s[64:65]
	s_mov_b32 m0, s63
	s_waitcnt vmcnt(8)
	s_waitcnt lgkmcnt(0)
	s_barrier
	s_setprio 1
	s_waitcnt lgkmcnt(6)
	v_mfma_f32_16x16x128_f8f6f4 v[94:97], v[18:25], v[180:187], v[94:97]
	v_mfma_f32_16x16x128_f8f6f4 v[90:93], v[26:33], v[180:187], v[90:93]
	s_waitcnt lgkmcnt(4)
	v_mfma_f32_16x16x128_f8f6f4 v[86:89], v[18:25], v[188:195], v[86:89]
	v_mfma_f32_16x16x128_f8f6f4 v[82:85], v[26:33], v[188:195], v[82:85]
	s_waitcnt lgkmcnt(2)
	v_mfma_f32_16x16x128_f8f6f4 v[78:81], v[18:25], v[196:203], v[78:81]
	v_mfma_f32_16x16x128_f8f6f4 v[74:77], v[26:33], v[196:203], v[74:77]
	s_waitcnt lgkmcnt(0)
	v_mfma_f32_16x16x128_f8f6f4 v[70:73], v[18:25], v[204:211], v[70:73]
	v_mfma_f32_16x16x128_f8f6f4 v[66:69], v[26:33], v[204:211], v[66:69]
	s_setprio 0
	s_setprio 1
	v_mfma_f32_16x16x128_f8f6f4 v[62:65], v[10:17], v[180:187], v[62:65]
	v_mfma_f32_16x16x128_f8f6f4 v[58:61], v[2:9], v[180:187], v[58:61]
	v_mfma_f32_16x16x128_f8f6f4 v[54:57], v[10:17], v[188:195], v[54:57]
	v_mfma_f32_16x16x128_f8f6f4 v[50:53], v[2:9], v[188:195], v[50:53]
	v_mfma_f32_16x16x128_f8f6f4 v[46:49], v[10:17], v[196:203], v[46:49]
	v_mfma_f32_16x16x128_f8f6f4 v[42:45], v[2:9], v[196:203], v[42:45]
	v_mfma_f32_16x16x128_f8f6f4 v[38:41], v[10:17], v[204:211], v[38:41]
	v_mfma_f32_16x16x128_f8f6f4 v[34:37], v[2:9], v[204:211], v[34:37]
	s_setprio 0
	s_barrier
	s_add_i32 s62, s62, 2
	s_add_u32 s26, s26, 0x100
	s_addc_u32 s27, s27, 0
	s_cmp_lt_u32 s62, 12
	s_cbranch_scc1 .LBB0_875
	v_readfirstlane_b32 s18, v230
	ds_read_b128 v[26:29], v172
	ds_read_b128 v[30:33], v172 offset:1024
	ds_read_b128 v[18:21], v172 offset:2048
	ds_read_b128 v[22:25], v172 offset:3072
	ds_read_b128 v[10:13], v173
	ds_read_b128 v[14:17], v173 offset:1024
	ds_read_b128 v[2:5], v173 offset:2048
	ds_read_b128 v[6:9], v173 offset:3072
	s_ashr_i32 s19, s18, 31
	s_lshl_b64 s[26:27], s[18:19], 22
	s_add_u32 s19, s35, s26
	s_addc_u32 s28, s36, s27
	s_ashr_i32 s15, s14, 31
	s_lshl_b64 s[26:27], s[14:15], 19
	s_add_u32 s26, s19, s26
	s_addc_u32 s27, s28, s27
	s_lshl_b64 s[28:29], s[16:17], 19
	s_and_b64 s[58:59], exec, s[2:3]
	s_cselect_b32 s25, s27, s25
	s_cselect_b32 s24, s26, s24
	s_cselect_b32 s15, s29, s23
	s_cselect_b32 s17, s28, s22
	ds_read_b128 v[180:183], v174
	ds_read_b128 v[184:187], v174 offset:1024
	ds_read_b128 v[188:191], v174 offset:2048
	ds_read_b128 v[192:195], v174 offset:3072
	ds_read_b128 v[196:199], v174 offset:4096
	ds_read_b128 v[200:203], v174 offset:5120
	ds_read_b128 v[204:207], v174 offset:6144
	ds_read_b128 v[208:211], v174 offset:7168
	s_add_u32 s22, s1, 0x40780
	s_addc_u32 s23, s57, 0
	s_add_u32 s58, s1, 0x60780
	s_addc_u32 s59, s57, 0
	s_mov_b32 s1, m0
	s_mov_b32 m0, s53
	s_nop 0
	global_load_lds_dwordx4 v167, s[22:23]
	s_mov_b32 m0, s54
	s_nop 0
	global_load_lds_dwordx4 v167, s[58:59]
	s_mov_b32 m0, s1
	s_waitcnt vmcnt(8)
	s_waitcnt lgkmcnt(0)
	s_barrier
; #define PG8_STAGEB(bufoff, gbase) glds2(voffB, (gbase), voffB, (gbase) + qstep, ldsb + (bufoff))
; #define PG8_STAGEA(bufoff, rowb, v, h, kb) do { if constexpr (GATHER) glds2((v)[h][0], Ab + (kb), (v)[h][1], Ab + (kb), ldsb + (bufoff)); \
;         else glds2(voffA, Ab + (rowb) + (h) * hstep + (kb), voffA, Ab + (rowb) + (h) * hstep + qstep + (kb), ldsb + (bufoff)); } while (0)
; #define PG8_LDA(dst, b, h) do { _Pragma("unroll") for (int m = 0; m < 4; ++m) _Pragma("unroll") for (int k = 0; k < 2; ++k) dst[m][k] = *(const PG8_LAS bf16x8*)(lds + PG8_SA(b, h) + aoff + m * 2048 + k * 1024); } while (0)
; #define PG8_LDB(dst, b, h) do { _Pragma("unroll") for (int n = 0; n < 2; ++n) _Pragma("unroll") for (int k = 0; k < 2; ++k) dst[n][k] = *(const PG8_LAS bf16x8*)(lds + PG8_SB(b, h) + boff + n * 2048 + k * 1024); } while (0)
; #define PG8_WAIT_V(n) asm volatile("s_waitcnt vmcnt(" #n ")" ::: "memory")
; #define PG8_WAIT_L(n) asm volatile("s_waitcnt lgkmcnt(" #n ")" ::: "memory")
; #define PG8_BAR __builtin_amdgcn_s_barrier()
; #define PG8_SCHED __builtin_amdgcn_sched_barrier(0)
; template <class Epi, bool GATHER, int MODE, bool SPLIT = false>
; __device__ __forceinline__ void gemm_phase(PG8_LAS unsigned char* lds, const Gemm g, const Order& S, const Epi& E) {
;     ...
;             PG8_WAIT_V(8); PG8_WAIT_L(0); PG8_BAR; PG8_MMA(1, 0, At, B0); PG8_MMA(1, 1, At, B1); PG8_BAR; PG8_SCHED;
;             PG8_LDB(B0, 1, 0); PG8_LDB(B1, 1, 1); PG8_SCHED; PG8_LDA(At, 1, 0); PG8_STAGEA(PG8_SA(0, 1), nAr, nv, 1, 0);
;             PG8_WAIT_V(8); PG8_WAIT_L(0); PG8_BAR; PG8_MMA(0, 0, At, B0); PG8_MMA(0, 1, At, B1); PG8_BAR; PG8_SCHED;
;             PG8_LDA(At, 1, 1); PG8_STAGEB(PG8_SB(1, 0), nB + kstep); PG8_STAGEB(PG8_SB(1, 1), nB + hstep + kstep); PG8_STAGEA(PG8_SA(1, 0), nAr, nv, 0, kstep);
	s_setprio 1
	s_waitcnt lgkmcnt(6)
	v_mfma_f32_16x16x128_f8f6f4 v[158:161], v[26:33], v[180:187], v[158:161]
	v_mfma_f32_16x16x128_f8f6f4 v[154:157], v[18:25], v[180:187], v[154:157]
	s_waitcnt lgkmcnt(4)
	v_mfma_f32_16x16x128_f8f6f4 v[150:153], v[26:33], v[188:195], v[150:153]
	v_mfma_f32_16x16x128_f8f6f4 v[146:149], v[18:25], v[188:195], v[146:149]
	s_waitcnt lgkmcnt(2)
	v_mfma_f32_16x16x128_f8f6f4 v[142:145], v[26:33], v[196:203], v[142:145]
	v_mfma_f32_16x16x128_f8f6f4 v[138:141], v[18:25], v[196:203], v[138:141]
	s_waitcnt lgkmcnt(0)
	v_mfma_f32_16x16x128_f8f6f4 v[134:137], v[26:33], v[204:211], v[134:137]
	v_mfma_f32_16x16x128_f8f6f4 v[130:133], v[18:25], v[204:211], v[130:133]
	s_setprio 0
	s_setprio 1
	v_mfma_f32_16x16x128_f8f6f4 v[126:129], v[10:17], v[180:187], v[126:129]
	v_mfma_f32_16x16x128_f8f6f4 v[122:125], v[2:9], v[180:187], v[122:125]
	v_mfma_f32_16x16x128_f8f6f4 v[118:121], v[10:17], v[188:195], v[118:121]
	v_mfma_f32_16x16x128_f8f6f4 v[114:117], v[2:9], v[188:195], v[114:117]
	v_mfma_f32_16x16x128_f8f6f4 v[110:113], v[10:17], v[196:203], v[110:113]
	v_mfma_f32_16x16x128_f8f6f4 v[106:109], v[2:9], v[196:203], v[106:109]
	v_mfma_f32_16x16x128_f8f6f4 v[102:105], v[10:17], v[204:211], v[102:105]
	v_mfma_f32_16x16x128_f8f6f4 v[98:101], v[2:9], v[204:211], v[98:101]
	s_setprio 0
	s_barrier
	s_add_u32 s22, s24, 0x20000
	s_addc_u32 s23, s25, 0
	ds_read_b128 v[180:183], v174 offset:16384
	ds_read_b128 v[184:187], v174 offset:17408
	ds_read_b128 v[188:191], v174 offset:18432
	ds_read_b128 v[192:195], v174 offset:19456
	ds_read_b128 v[196:199], v174 offset:20480
	ds_read_b128 v[200:203], v174 offset:21504
	ds_read_b128 v[204:207], v174 offset:22528
	ds_read_b128 v[208:211], v174 offset:23552
	s_mov_b32 s1, m0
	s_mov_b32 m0, s21
	s_nop 0
	global_load_lds_dwordx4 v166, s[24:25]
	s_mov_b32 m0, s41
	s_nop 0
	global_load_lds_dwordx4 v166, s[22:23]
	s_mov_b32 m0, s1
	s_add_u32 s22, s24, 0x40000
	s_addc_u32 s23, s25, 0
	s_add_u32 s58, s24, 0x60000
	s_addc_u32 s59, s25, 0
	s_mov_b32 s1, m0
	s_mov_b32 m0, s42
	s_nop 0
	global_load_lds_dwordx4 v166, s[22:23]
	s_mov_b32 m0, s43
	s_nop 0
	global_load_lds_dwordx4 v166, s[58:59]
	s_mov_b32 m0, s1
	s_add_u32 s22, s31, s17
	s_addc_u32 s23, s34, s15
	s_add_u32 s58, s22, 0x20000
	s_addc_u32 s59, s23, 0
	s_mov_b32 s1, m0
	s_mov_b32 m0, s37
	s_nop 0
	global_load_lds_dwordx4 v167, s[22:23]
	s_mov_b32 m0, s44
	s_nop 0
	global_load_lds_dwordx4 v167, s[58:59]
	s_mov_b32 m0, s1
	s_waitcnt vmcnt(8)
	s_waitcnt lgkmcnt(0)
	s_barrier
	s_setprio 1
	s_waitcnt lgkmcnt(6)
	v_mfma_f32_16x16x128_f8f6f4 v[94:97], v[26:33], v[180:187], v[94:97]
	v_mfma_f32_16x16x128_f8f6f4 v[90:93], v[18:25], v[180:187], v[90:93]
	s_waitcnt lgkmcnt(4)
	v_mfma_f32_16x16x128_f8f6f4 v[86:89], v[26:33], v[188:195], v[86:89]
	v_mfma_f32_16x16x128_f8f6f4 v[82:85], v[18:25], v[188:195], v[82:85]
	s_waitcnt lgkmcnt(2)
	v_mfma_f32_16x16x128_f8f6f4 v[78:81], v[26:33], v[196:203], v[78:81]
	v_mfma_f32_16x16x128_f8f6f4 v[74:77], v[18:25], v[196:203], v[74:77]
	s_waitcnt lgkmcnt(0)
	v_mfma_f32_16x16x128_f8f6f4 v[70:73], v[26:33], v[204:211], v[70:73]
	v_mfma_f32_16x16x128_f8f6f4 v[66:69], v[18:25], v[204:211], v[66:69]
	s_setprio 0
	s_setprio 1
	v_mfma_f32_16x16x128_f8f6f4 v[62:65], v[10:17], v[180:187], v[62:65]
	v_mfma_f32_16x16x128_f8f6f4 v[58:61], v[2:9], v[180:187], v[58:61]
	v_mfma_f32_16x16x128_f8f6f4 v[54:57], v[10:17], v[188:195], v[54:57]
	v_mfma_f32_16x16x128_f8f6f4 v[50:53], v[2:9], v[188:195], v[50:53]
	v_mfma_f32_16x16x128_f8f6f4 v[46:49], v[10:17], v[196:203], v[46:49]
	v_mfma_f32_16x16x128_f8f6f4 v[42:45], v[2:9], v[196:203], v[42:45]
	v_mfma_f32_16x16x128_f8f6f4 v[38:41], v[10:17], v[204:211], v[38:41]
	v_mfma_f32_16x16x128_f8f6f4 v[34:37], v[2:9], v[204:211], v[34:37]
	s_setprio 0
	s_barrier
	ds_read_b128 v[26:29], v175
	ds_read_b128 v[30:33], v175 offset:1024
	ds_read_b128 v[18:21], v175 offset:2048
	ds_read_b128 v[22:25], v175 offset:3072
	ds_read_b128 v[10:13], v176
	ds_read_b128 v[14:17], v176 offset:1024
	ds_read_b128 v[2:5], v176 offset:2048
	ds_read_b128 v[6:9], v176 offset:3072
	ds_read_b128 v[180:183], v174 offset:32768
	ds_read_b128 v[184:187], v174 offset:33792
	ds_read_b128 v[188:191], v174 offset:34816
	ds_read_b128 v[192:195], v174 offset:35840
	ds_read_b128 v[196:199], v174 offset:36864
	ds_read_b128 v[200:203], v174 offset:37888
	ds_read_b128 v[204:207], v174 offset:38912
	ds_read_b128 v[208:211], v174 offset:39936
	s_add_u32 s58, s22, 0x40000
	s_addc_u32 s59, s23, 0
	s_add_u32 s60, s22, 0x60000
	s_addc_u32 s61, s23, 0
	s_mov_b32 s1, m0
	s_mov_b32 m0, s45
	s_nop 0
	global_load_lds_dwordx4 v167, s[58:59]
	s_mov_b32 m0, s46
	s_nop 0
	global_load_lds_dwordx4 v167, s[60:61]
	s_mov_b32 m0, s1
	s_waitcnt vmcnt(8)
	s_waitcnt lgkmcnt(0)
	s_barrier
; #define PG8_STAGEB(bufoff, gbase) glds2(voffB, (gbase), voffB, (gbase) + qstep, ldsb + (bufoff))
; #define PG8_STAGEA(bufoff, rowb, v, h, kb) do { if constexpr (GATHER) glds2((v)[h][0], Ab + (kb), (v)[h][1], Ab + (kb), ldsb + (bufoff)); \
;         else glds2(voffA, Ab + (rowb) + (h) * hstep + (kb), voffA, Ab + (rowb) + (h) * hstep + qstep + (kb), ldsb + (bufoff)); } while (0)
; #define PG8_LDA(dst, b, h) do { _Pragma("unroll") for (int m = 0; m < 4; ++m) _Pragma("unroll") for (int k = 0; k < 2; ++k) dst[m][k] = *(const PG8_LAS bf16x8*)(lds + PG8_SA(b, h) + aoff + m * 2048 + k * 1024); } while (0)
; #define PG8_WAIT_V(n) asm volatile("s_waitcnt vmcnt(" #n ")" ::: "memory")
; #define PG8_WAIT_L(n) asm volatile("s_waitcnt lgkmcnt(" #n ")" ::: "memory")
; #define PG8_BAR __builtin_amdgcn_s_barrier()
; #define PG8_SCHED __builtin_amdgcn_sched_barrier(0)
; template <class Epi, bool GATHER, int MODE, bool SPLIT = false>
; __device__ __forceinline__ void gemm_phase(PG8_LAS unsigned char* lds, const Gemm g, const Order& S, const Epi& E) {
;     ...
;             PG8_LDA(At, 1, 1); PG8_STAGEB(PG8_SB(1, 0), nB + kstep); PG8_STAGEB(PG8_SB(1, 1), nB + hstep + kstep); PG8_STAGEA(PG8_SA(1, 0), nAr, nv, 0, kstep);
;             PG8_WAIT_V(8); PG8_WAIT_L(0); PG8_BAR; PG8_MMA(1, 0, At, B0); PG8_MMA(1, 1, At, B1); PG8_BAR; PG8_SCHED;
;         }
;         if (wr == 0) PG8_BAR;
	s_setprio 1
	s_waitcnt lgkmcnt(6)
	v_mfma_f32_16x16x128_f8f6f4 v[158:161], v[26:33], v[180:187], v[158:161]
	v_mfma_f32_16x16x128_f8f6f4 v[154:157], v[18:25], v[180:187], v[154:157]
	s_waitcnt lgkmcnt(4)
	v_mfma_f32_16x16x128_f8f6f4 v[150:153], v[26:33], v[188:195], v[150:153]
	v_mfma_f32_16x16x128_f8f6f4 v[146:149], v[18:25], v[188:195], v[146:149]
	s_waitcnt lgkmcnt(2)
	v_mfma_f32_16x16x128_f8f6f4 v[142:145], v[26:33], v[196:203], v[142:145]
	v_mfma_f32_16x16x128_f8f6f4 v[138:141], v[18:25], v[196:203], v[138:141]
	s_waitcnt lgkmcnt(0)
	v_mfma_f32_16x16x128_f8f6f4 v[134:137], v[26:33], v[204:211], v[134:137]
	v_mfma_f32_16x16x128_f8f6f4 v[130:133], v[18:25], v[204:211], v[130:133]
	s_setprio 0
	s_setprio 1
	v_mfma_f32_16x16x128_f8f6f4 v[126:129], v[10:17], v[180:187], v[126:129]
	v_mfma_f32_16x16x128_f8f6f4 v[122:125], v[2:9], v[180:187], v[122:125]
	v_mfma_f32_16x16x128_f8f6f4 v[118:121], v[10:17], v[188:195], v[118:121]
	v_mfma_f32_16x16x128_f8f6f4 v[114:117], v[2:9], v[188:195], v[114:117]
	v_mfma_f32_16x16x128_f8f6f4 v[110:113], v[10:17], v[196:203], v[110:113]
	v_mfma_f32_16x16x128_f8f6f4 v[106:109], v[2:9], v[196:203], v[106:109]
	v_mfma_f32_16x16x128_f8f6f4 v[102:105], v[10:17], v[204:211], v[102:105]
	v_mfma_f32_16x16x128_f8f6f4 v[98:101], v[2:9], v[204:211], v[98:101]
	s_setprio 0
	s_barrier
	s_add_u32 s58, s24, 0x80
	s_addc_u32 s59, s25, 0
	s_add_u32 s60, s24, 0x20080
	s_addc_u32 s61, s25, 0
	ds_read_b128 v[180:183], v174 offset:49152
	ds_read_b128 v[184:187], v174 offset:50176
	ds_read_b128 v[188:191], v174 offset:51200
	ds_read_b128 v[192:195], v174 offset:52224
	ds_read_b128 v[196:199], v174 offset:53248
	ds_read_b128 v[200:203], v174 offset:54272
	ds_read_b128 v[204:207], v174 offset:55296
	ds_read_b128 v[208:211], v174 offset:56320
	s_mov_b32 s1, m0
	s_mov_b32 m0, s47
	s_nop 0
	global_load_lds_dwordx4 v166, s[58:59]
	s_mov_b32 m0, s48
	s_nop 0
	global_load_lds_dwordx4 v166, s[60:61]
	s_mov_b32 m0, s1
	s_add_u32 s58, s24, 0x40080
	s_addc_u32 s59, s25, 0
	s_add_u32 s24, s24, 0x60080
	s_addc_u32 s25, s25, 0
	s_mov_b32 s1, m0
	s_mov_b32 m0, s51
	s_nop 0
	global_load_lds_dwordx4 v166, s[58:59]
	s_mov_b32 m0, s52
	s_nop 0
	global_load_lds_dwordx4 v166, s[24:25]
	s_mov_b32 m0, s1
	s_add_u32 s24, s22, 0x80
	s_addc_u32 s25, s23, 0
	s_add_u32 s22, s22, 0x20080
	s_addc_u32 s23, s23, 0
	s_mov_b32 s1, m0
	s_mov_b32 m0, s49
	s_nop 0
	global_load_lds_dwordx4 v167, s[24:25]
	s_mov_b32 m0, s50
	s_nop 0
	global_load_lds_dwordx4 v167, s[22:23]
	s_mov_b32 m0, s1
	s_waitcnt vmcnt(8)
	s_waitcnt lgkmcnt(0)
	s_barrier
	s_setprio 1
	s_waitcnt lgkmcnt(6)
	v_mfma_f32_16x16x128_f8f6f4 v[94:97], v[26:33], v[180:187], v[94:97]
	v_mfma_f32_16x16x128_f8f6f4 v[90:93], v[18:25], v[180:187], v[90:93]
	s_waitcnt lgkmcnt(4)
	v_mfma_f32_16x16x128_f8f6f4 v[86:89], v[26:33], v[188:195], v[86:89]
	v_mfma_f32_16x16x128_f8f6f4 v[82:85], v[18:25], v[188:195], v[82:85]
	s_waitcnt lgkmcnt(2)
	v_mfma_f32_16x16x128_f8f6f4 v[78:81], v[26:33], v[196:203], v[78:81]
	v_mfma_f32_16x16x128_f8f6f4 v[74:77], v[18:25], v[196:203], v[74:77]
	s_waitcnt lgkmcnt(0)
	v_mfma_f32_16x16x128_f8f6f4 v[70:73], v[26:33], v[204:211], v[70:73]
	v_mfma_f32_16x16x128_f8f6f4 v[66:69], v[18:25], v[204:211], v[66:69]
	s_setprio 0
	s_setprio 1
	v_mfma_f32_16x16x128_f8f6f4 v[62:65], v[10:17], v[180:187], v[62:65]
	v_mfma_f32_16x16x128_f8f6f4 v[58:61], v[2:9], v[180:187], v[58:61]
	v_mfma_f32_16x16x128_f8f6f4 v[54:57], v[10:17], v[188:195], v[54:57]
	v_mfma_f32_16x16x128_f8f6f4 v[50:53], v[2:9], v[188:195], v[50:53]
	v_mfma_f32_16x16x128_f8f6f4 v[46:49], v[10:17], v[196:203], v[46:49]
	v_mfma_f32_16x16x128_f8f6f4 v[42:45], v[2:9], v[196:203], v[42:45]
	v_mfma_f32_16x16x128_f8f6f4 v[38:41], v[10:17], v[204:211], v[38:41]
	v_mfma_f32_16x16x128_f8f6f4 v[34:37], v[2:9], v[204:211], v[34:37]
	s_setprio 0
	s_nop 0
	s_andn2_b64 vcc, exec, s[8:9]
	s_cbranch_vccnz .LBB0_878
	s_barrier
